# rank-phase stream 15 tiles per workgroup, attention-phase converter streams 6 more each
# baseline (speedup 1.0000x reference)
; DEVI int opaque_tid() { int t = threadIdx.x; asm volatile("" : "+v"(t)); return t; }
; DEVI void cvt8_load(const Params& p, int L, int t, CvtIn& in) {
;     const int which = t / 4096, r = t % 4096, le = L * 16 + r / 256, kt = (r % 256) / 16, nt = r % 16;
;     const float* src = (which == 2 ? p.w_down : (which == 0 ? p.w_gate : p.w_up)) + (size_t)le * 2048 * 2048;
;     const int tid = opaque_tid(), nq = tid & 31, kq0 = tid >> 5;
; #pragma unroll
;     for (int it = 0; it < 2; ++it)
; #pragma unroll
;         for (int kk = 0; kk < 4; ++kk) in.v[it * 4 + kk] = __builtin_nontemporal_load((const f32x4*)(src + (size_t)(kt * 128 + (kq0 + it * 16) * 4 + kk) * 2048 + nt * 128 + nq * 4));
; }
; DEVI void cvt8_stream3(const Params& p, int L, int t0, int step, int count, char* smem) {
;     if (count <= 0) return;
;     CvtIn a, b; cvt8_load(p, L, t0, a);
;     if (count > 1) cvt8_load(p, L, t0 + step, b);
.LBB0_773:
	s_and_b64 vcc, exec, s[16:17]
	s_cbranch_vccz .LBB0_801
	v_readlane_b32 s4, v255, 0
	v_readlane_b32 s5, v255, 1
	s_mov_b32 s6, s2
	s_mov_b64 s[16:17], -1
	s_and_b64 vcc, exec, s[4:5]
	s_cbranch_vccz .LBB0_784
	s_add_i32 s7, s6, 0x1c10
	s_and_b32 s4, s7, 0xfffff000
	s_add_i32 s5, s6, 0x2c0f
	s_cmpk_lt_u32 s5, 0x1fff
	s_cselect_b32 s5, s64, 0x80
	s_cmpk_lg_i32 s4, 0x2000
	s_cselect_b32 s4, s5, 0x88
	s_add_u32 s4, s0, s4
	s_addc_u32 s5, s1, 0
	s_ashr_i32 s14, s7, 31
	s_lshr_b32 s14, s14, 20
	s_add_i32 s14, s7, s14
	s_and_b32 s14, s14, 0xf000
	s_sub_i32 s7, s7, s14
	s_sext_i32_i16 s14, s7
	s_lshr_b32 s14, s14, 15
	s_bfe_u32 s16, s14, 0x4000c
	s_add_i32 s16, s7, s16
	s_and_b32 s16, s16, 0xfff0
	s_bfe_u32 s14, s14, 0x80008
	s_sub_i32 s16, s7, s16
	s_add_i32 s14, s7, s14
	s_sext_i32_i16 s18, s16
	s_sext_i32_i16 s16, s14
	s_and_b32 s14, s14, 0xff00
	s_load_dwordx2 s[4:5], s[4:5], 0x0
	s_ashr_i32 s16, s16, 8
	s_sub_i32 s7, s7, s14
	s_sext_i32_i16 s14, s7
	s_add_i32 s16, s16, 16
	s_bfe_u32 s14, s14, 0x4001b
	s_and_b32 s52, s16, 0xffff
	s_add_i32 s7, s7, s14
	s_lshl_b64 s[16:17], s[52:53], 24
	s_sext_i32_i16 s7, s7
	s_waitcnt lgkmcnt(0)
	s_add_u32 s14, s4, s16
	v_mov_b32_e32 v1, v0
	s_addc_u32 s16, s5, s17
	s_lshl_b32 s4, s7, 3
	v_ashrrev_i32_e32 v2, 3, v1
	s_and_b32 s4, s4, 0xffffff80
	v_and_b32_e32 v2, -4, v2
	s_waitcnt vmcnt(2)
	v_add_u32_e32 v4, s4, v2
	s_lshl_b32 s4, s18, 7
	s_ashr_i32 s5, s4, 31
	s_lshl_b64 s[4:5], s[4:5], 2
	s_add_u32 s4, s14, s4
	v_lshlrev_b32_e32 v1, 4, v1
	s_addc_u32 s5, s16, s5
	v_and_b32_e32 v2, 0x1f0, v1
	v_ashrrev_i32_e32 v5, 31, v4
	v_lshl_add_u64 v[6:7], s[4:5], 0, v[2:3]
	s_waitcnt vmcnt(1)
	v_lshlrev_b64 v[8:9], 13, v[4:5]
	v_lshl_add_u64 v[12:13], v[6:7], 0, v[8:9]
	v_or_b32_e32 v8, 1, v4
	v_ashrrev_i32_e32 v9, 31, v8
	v_lshlrev_b64 v[8:9], 13, v[8:9]
	v_lshl_add_u64 v[8:9], v[6:7], 0, v[8:9]
	global_load_dwordx4 v[20:23], v[12:13], off nt
	global_load_dwordx4 v[24:27], v[8:9], off nt
	v_or_b32_e32 v8, 2, v4
	v_or_b32_e32 v4, 3, v4
	v_ashrrev_i32_e32 v9, 31, v8
	v_ashrrev_i32_e32 v5, 31, v4
	v_lshlrev_b64 v[8:9], 13, v[8:9]
	v_lshlrev_b64 v[4:5], 13, v[4:5]
	v_lshl_add_u64 v[8:9], v[6:7], 0, v[8:9]
	v_lshl_add_u64 v[4:5], v[6:7], 0, v[4:5]
	global_load_dwordx4 v[28:31], v[8:9], off nt
	global_load_dwordx4 v[32:35], v[4:5], off nt
	v_add_co_u32_e32 v4, vcc, s94, v12
	s_mov_b32 s19, 0x82000
	s_nop 0
	v_addc_co_u32_e32 v5, vcc, 0, v13, vcc
	v_add_co_u32_e32 v8, vcc, s19, v12
	s_mov_b32 s4, 0x84000
	s_nop 0
	v_addc_co_u32_e32 v9, vcc, 0, v13, vcc
	v_add_co_u32_e32 v14, vcc, s4, v12
	s_mov_b32 s4, 0x86000
	s_nop 0
	v_addc_co_u32_e32 v15, vcc, 0, v13, vcc
	s_add_i32 s7, s6, 0x1c30
	v_add_co_u32_e32 v16, vcc, s4, v12
	s_and_b32 s4, s7, 0xfffff000
	s_add_i32 s5, s6, 0x2c2f
	s_cmpk_lt_u32 s5, 0x1fff
	s_cselect_b32 s5, s64, 0x80
	s_cmpk_lg_i32 s4, 0x2000
	s_cselect_b32 s4, s5, 0x88
	s_add_u32 s4, s0, s4
	s_addc_u32 s5, s1, 0
	s_ashr_i32 s14, s7, 31
	s_lshr_b32 s14, s14, 20
	s_add_i32 s14, s7, s14
	s_and_b32 s14, s14, 0xf000
	s_sub_i32 s7, s7, s14
	s_sext_i32_i16 s14, s7
	s_lshr_b32 s14, s14, 15
	s_bfe_u32 s16, s14, 0x4000c
	s_add_i32 s16, s7, s16
	s_and_b32 s16, s16, 0xfff0
	s_bfe_u32 s14, s14, 0x80008
	v_addc_co_u32_e32 v17, vcc, 0, v13, vcc
	s_sub_i32 s16, s7, s16
	s_add_i32 s14, s7, s14
	global_load_dwordx4 v[4:7], v[4:5], off nt
	s_nop 0
	global_load_dwordx4 v[8:11], v[8:9], off nt
	s_nop 0
	global_load_dwordx4 v[12:15], v[14:15], off nt
	s_nop 0
	global_load_dwordx4 v[16:19], v[16:17], off nt
	s_sext_i32_i16 s18, s16
	s_sext_i32_i16 s16, s14
	s_and_b32 s14, s14, 0xff00
	s_load_dwordx2 s[4:5], s[4:5], 0x0
	s_ashr_i32 s16, s16, 8
	s_sub_i32 s7, s7, s14
	s_sext_i32_i16 s14, s7
	s_add_i32 s16, s16, 16
	s_bfe_u32 s14, s14, 0x4001b
	s_and_b32 s52, s16, 0xffff
	s_add_i32 s7, s7, s14
	s_lshl_b64 s[16:17], s[52:53], 24
	s_sext_i32_i16 s7, s7
	s_waitcnt lgkmcnt(0)
	s_add_u32 s14, s4, s16
	v_mov_b32_e32 v1, v0
	s_addc_u32 s16, s5, s17
	s_lshl_b32 s4, s7, 3
	v_ashrrev_i32_e32 v2, 3, v1
	s_and_b32 s4, s4, 0xffffff80
	v_and_b32_e32 v2, -4, v2
	v_add_u32_e32 v44, s4, v2
	s_lshl_b32 s4, s18, 7
	s_ashr_i32 s5, s4, 31
	s_lshl_b64 s[4:5], s[4:5], 2
	s_add_u32 s4, s14, s4
	v_lshlrev_b32_e32 v1, 4, v1
	s_addc_u32 s5, s16, s5
	v_and_b32_e32 v2, 0x1f0, v1
	v_ashrrev_i32_e32 v45, 31, v44
	v_lshl_add_u64 v[46:47], s[4:5], 0, v[2:3]
	v_lshlrev_b64 v[36:37], 13, v[44:45]
	v_lshl_add_u64 v[48:49], v[46:47], 0, v[36:37]
	v_or_b32_e32 v36, 1, v44
	v_or_b32_e32 v50, 2, v44
	v_or_b32_e32 v44, 3, v44
	v_ashrrev_i32_e32 v37, 31, v36
	v_ashrrev_i32_e32 v51, 31, v50
	v_ashrrev_i32_e32 v45, 31, v44
	v_lshlrev_b64 v[36:37], 13, v[36:37]
	v_lshlrev_b64 v[50:51], 13, v[50:51]
	v_lshlrev_b64 v[44:45], 13, v[44:45]
	v_lshl_add_u64 v[40:41], v[46:47], 0, v[36:37]
	v_lshl_add_u64 v[50:51], v[46:47], 0, v[50:51]
	v_lshl_add_u64 v[44:45], v[46:47], 0, v[44:45]
	global_load_dwordx4 v[36:39], v[48:49], off nt
	s_nop 0
	global_load_dwordx4 v[40:43], v[40:41], off nt
	s_nop 0
	global_load_dwordx4 v[72:75], v[50:51], off nt
	global_load_dwordx4 v[76:79], v[44:45], off nt
	v_add_co_u32_e32 v44, vcc, s94, v48
	s_mov_b32 s4, 0
	s_nop 0
	v_addc_co_u32_e32 v45, vcc, 0, v49, vcc
	v_add_co_u32_e32 v46, vcc, s19, v48
	s_add_i32 s5, s6, 0x2c4f
	s_nop 0
	v_addc_co_u32_e32 v47, vcc, 0, v49, vcc
	global_load_dwordx4 v[84:87], v[44:45], off nt
	global_load_dwordx4 v[88:91], v[46:47], off nt
	v_add_co_u32_e32 v44, vcc, 0x84000, v48
	s_nop 1
	v_addc_co_u32_e32 v45, vcc, 0, v49, vcc
	v_add_co_u32_e32 v46, vcc, 0x86000, v48
	s_nop 1
	v_addc_co_u32_e32 v47, vcc, 0, v49, vcc
	global_load_dwordx4 v[92:95], v[44:45], off nt
	global_load_dwordx4 v[96:99], v[46:47], off nt
	s_branch .LBB0_777
; DEVI int opaque_tid() { int t = threadIdx.x; asm volatile("" : "+v"(t)); return t; }
; DEVI unsigned cvt4_fp8(float a, float b, float c, float d) { int w = 0; w = __builtin_amdgcn_cvt_pk_fp8_f32(a, b, w, false); w = __builtin_amdgcn_cvt_pk_fp8_f32(c, d, w, true); return (unsigned)w; }
; DEVI void cvt8_finish(const Params& p, int L, int t, const CvtIn& in, char* smem) {
;     const int which = t / 4096, r = t % 4096, le = L * 16 + r / 256, kt = (r % 256) / 16, nt = r % 16;
;     unsigned char* dst = (which == 2) ? (unsigned char*)(p.ws + WS_WDN) + (size_t)le * 2048 * 2048 + (size_t)(nt * 128) * 2048
;                                       : (unsigned char*)(p.ws + WS_WGU) + (size_t)le * 4096 * 2048 + (size_t)(nt * 256 + which * 128) * 2048;
;     unsigned char* T = (unsigned char*)smem;
;     const int tid = opaque_tid(), nq = tid & 31, kq0 = tid >> 5;
; #pragma unroll
;     for (int it = 0; it < 2; ++it) { const int kq = kq0 + it * 16;
; #pragma unroll
;         for (int j = 0; j < 4; ++j) *(unsigned*)(T + (nq * 4 + j) * 144 + kq * 4) =
;             cvt4_fp8(in.v[it * 4][j] * W8_SCALE, in.v[it * 4 + 1][j] * W8_SCALE, in.v[it * 4 + 2][j] * W8_SCALE, in.v[it * 4 + 3][j] * W8_SCALE); }
;     __syncthreads();
; #pragma unroll
;     for (int i = 0; i < 2; ++i) { const int nl = (tid >> 3) + 64 * i, kc = (tid & 7) * 16;
;         *(u32x4*)(dst + (size_t)nl * 2048 + kt * 128 + kc) = *(const u32x4*)(T + nl * 144 + kc); }
;     __syncthreads();
; }
; DEVI void cvt8_stream3(const Params& p, int L, int t0, int step, int count, char* smem) {
;     ...
; #pragma nounroll
;     for (int i = 0; i < count; ++i) { CvtIn c;
;         if (i + 2 < count) cvt8_load(p, L, t0 + (i + 2) * step, c);
;         cvt8_finish(p, L, t0 + i * step, a, smem);
;         a = b; b = c; }
.LBB0_776:
	v_mul_f32_e32 v20, 0x42800000, v20
	v_mul_f32_e32 v24, 0x42800000, v24
	v_mov_b32_e32 v101, v3
	v_cvt_pk_fp8_f32 v101, v20, v24
	v_mul_f32_e32 v24, 0x42800000, v28
	v_mul_f32_e32 v28, 0x42800000, v32
	v_mov_b32_e32 v1, v0
	v_cvt_pk_fp8_f32 v101, v24, v28 op_sel:[0,0,1]
	v_mul_f32_e32 v21, 0x42800000, v21
	v_mul_f32_e32 v24, 0x42800000, v25
	v_mov_b32_e32 v25, v3
	v_cvt_pk_fp8_f32 v25, v21, v24
	v_lshlrev_b32_e32 v2, 2, v1
	v_and_b32_e32 v2, 0x7c, v2
	v_ashrrev_i32_e32 v100, 3, v1
	v_and_b32_e32 v20, -4, v100
	v_mul_u32_u24_e32 v2, 0x90, v2
	v_add3_u32 v2, 0, v20, v2
	v_mul_f32_e32 v20, 0x42800000, v29
	v_mul_f32_e32 v21, 0x42800000, v33
	v_cvt_pk_fp8_f32 v25, v20, v21 op_sel:[0,0,1]
	v_mul_f32_e32 v20, 0x42800000, v22
	v_mul_f32_e32 v21, 0x42800000, v26
	v_mov_b32_e32 v26, v3
	v_cvt_pk_fp8_f32 v26, v20, v21
	v_mul_f32_e32 v20, 0x42800000, v23
	v_mul_f32_e32 v21, 0x42800000, v27
	v_mov_b32_e32 v23, v3
	v_cvt_pk_fp8_f32 v23, v20, v21
	v_mul_f32_e32 v20, 0x42800000, v31
	v_mul_f32_e32 v21, 0x42800000, v35
	v_mul_f32_e32 v4, 0x42800000, v4
	v_cvt_pk_fp8_f32 v23, v20, v21 op_sel:[0,0,1]
	v_mul_f32_e32 v8, 0x42800000, v8
	v_mov_b32_e32 v20, v3
	v_cvt_pk_fp8_f32 v20, v4, v8
	v_mul_f32_e32 v4, 0x42800000, v5
	v_mul_f32_e32 v5, 0x42800000, v9
	v_mov_b32_e32 v8, v3
	v_cvt_pk_fp8_f32 v8, v4, v5
	s_lshl_b32 s14, s14, 8
	v_mul_f32_e32 v4, 0x42800000, v13
	v_mul_f32_e32 v5, 0x42800000, v17
	s_sub_i32 s7, s7, s14
	v_cvt_pk_fp8_f32 v8, v4, v5 op_sel:[0,0,1]
	v_mul_f32_e32 v4, 0x42800000, v6
	v_mul_f32_e32 v5, 0x42800000, v10
	v_mov_b32_e32 v10, v3
	s_sext_i32_i16 s14, s7
	v_cvt_pk_fp8_f32 v10, v4, v5
	v_mul_f32_e32 v4, 0x42800000, v7
	v_mul_f32_e32 v5, 0x42800000, v11
	v_mov_b32_e32 v7, v3
	s_bfe_u32 s14, s14, 0x4001b
	v_mul_f32_e32 v12, 0x42800000, v12
	v_mul_f32_e32 v16, 0x42800000, v16
	v_cvt_pk_fp8_f32 v7, v4, v5
	s_add_i32 s7, s7, s14
	v_cvt_pk_fp8_f32 v20, v12, v16 op_sel:[0,0,1]
	s_sext_i32_i16 s7, s7
	v_mul_f32_e32 v22, 0x42800000, v30
	v_mul_f32_e32 v24, 0x42800000, v34
	v_mul_f32_e32 v6, 0x42800000, v14
	v_mul_f32_e32 v9, 0x42800000, v18
	v_cvt_pk_fp8_f32 v26, v22, v24 op_sel:[0,0,1]
	v_cvt_pk_fp8_f32 v10, v6, v9 op_sel:[0,0,1]
	v_mul_f32_e32 v4, 0x42800000, v15
	v_mul_f32_e32 v5, 0x42800000, v19
	s_lshl_b32 s7, s7, 3
	v_cvt_pk_fp8_f32 v7, v4, v5 op_sel:[0,0,1]
	v_lshlrev_b32_e32 v1, 4, v1
	s_and_b32 s7, s7, 0xffffff80
	ds_write2_b32 v2, v101, v20 offset1:16
	ds_write2_b32 v2, v25, v8 offset0:36 offset1:52
	ds_write2_b32 v2, v26, v10 offset0:72 offset1:88
	ds_write2_b32 v2, v23, v7 offset0:108 offset1:124
	v_and_b32_e32 v2, 0x70, v1
	s_ashr_i32 s14, s7, 31
	v_mul_lo_u32 v1, v100, s91
	s_add_u32 s16, s16, s7
	v_add3_u32 v1, 0, v2, v1
	s_waitcnt lgkmcnt(0)
	s_barrier
	s_addc_u32 s17, s17, s14
	ds_read_b128 v[4:7], v1
	v_ashrrev_i32_e32 v101, 31, v100
	v_lshl_add_u64 v[8:9], s[16:17], 0, v[2:3]
	v_lshlrev_b64 v[10:11], 11, v[100:101]
	v_lshl_add_u64 v[12:13], v[8:9], 0, v[10:11]
	ds_read_b128 v[8:11], v1 offset:9216
	s_waitcnt lgkmcnt(1)
	global_store_dwordx4 v[12:13], v[4:7], off
	s_add_i32 s4, s4, 1
	s_add_i32 s5, s5, 32
	v_add_co_u32_e32 v4, vcc, 0x20000, v12
	v_mov_b64_e32 v[20:21], v[80:81]
	s_nop 0
	v_addc_co_u32_e32 v5, vcc, 0, v13, vcc
	s_waitcnt lgkmcnt(0)
	global_store_dwordx4 v[4:5], v[8:11], off
	v_mov_b64_e32 v[24:25], v[68:69]
	v_mov_b64_e32 v[28:29], v[64:65]
	v_mov_b64_e32 v[32:33], v[60:61]
	v_mov_b64_e32 v[4:5], v[56:57]
	v_mov_b64_e32 v[8:9], v[52:53]
	v_mov_b64_e32 v[12:13], v[48:49]
	v_mov_b64_e32 v[16:17], v[44:45]
	s_cmpk_eq_i32 s4, 0x54
	v_mov_b64_e32 v[22:23], v[82:83]
	v_mov_b64_e32 v[26:27], v[70:71]
	v_mov_b64_e32 v[30:31], v[66:67]
	v_mov_b64_e32 v[34:35], v[62:63]
	v_mov_b64_e32 v[6:7], v[58:59]
	v_mov_b64_e32 v[10:11], v[54:55]
	v_mov_b64_e32 v[14:15], v[50:51]
	v_mov_b64_e32 v[18:19], v[46:47]
	s_barrier
	s_cbranch_scc1 .LBB0_783
; DEVI int opaque_tid() { int t = threadIdx.x; asm volatile("" : "+v"(t)); return t; }
; DEVI void cvt8_load(const Params& p, int L, int t, CvtIn& in) {
;     const int which = t / 4096, r = t % 4096, le = L * 16 + r / 256, kt = (r % 256) / 16, nt = r % 16;
;     const float* src = (which == 2 ? p.w_down : (which == 0 ? p.w_gate : p.w_up)) + (size_t)le * 2048 * 2048;
;     const int tid = opaque_tid(), nq = tid & 31, kq0 = tid >> 5;
; #pragma unroll
;     for (int it = 0; it < 2; ++it)
; #pragma unroll
;         for (int kk = 0; kk < 4; ++kk) in.v[it * 4 + kk] = __builtin_nontemporal_load((const f32x4*)(src + (size_t)(kt * 128 + (kq0 + it * 16) * 4 + kk) * 2048 + nt * 128 + nq * 4));
; }
; DEVI void cvt8_stream3(const Params& p, int L, int t0, int step, int count, char* smem) {
;     ...
; #pragma nounroll
;     for (int i = 0; i < count; ++i) { CvtIn c;
;         if (i + 2 < count) cvt8_load(p, L, t0 + (i + 2) * step, c);
;         cvt8_finish(p, L, t0 + i * step, a, smem);
;         a = b; b = c; }
.LBB0_777:
	s_waitcnt vmcnt(0)
	v_mov_b64_e32 v[44:45], v[96:97]
	v_mov_b64_e32 v[48:49], v[92:93]
	v_mov_b64_e32 v[52:53], v[88:89]
	v_mov_b64_e32 v[56:57], v[84:85]
	v_mov_b64_e32 v[60:61], v[76:77]
	v_mov_b64_e32 v[64:65], v[72:73]
	v_mov_b64_e32 v[70:71], v[42:43]
	v_mov_b64_e32 v[82:83], v[38:39]
	v_mov_b64_e32 v[46:47], v[98:99]
	v_mov_b64_e32 v[50:51], v[94:95]
	v_mov_b64_e32 v[54:55], v[90:91]
	v_mov_b64_e32 v[58:59], v[86:87]
	v_mov_b64_e32 v[62:63], v[78:79]
	v_mov_b64_e32 v[66:67], v[74:75]
	v_mov_b64_e32 v[68:69], v[40:41]
	s_cmpk_gt_u32 s4, 0x51
	v_mov_b64_e32 v[80:81], v[36:37]
	s_cbranch_scc1 .LBB0_779
	s_add_i32 s7, s5, 0xfffff001
	s_and_b32 s14, s7, 0xfffff000
	s_cmpk_lt_u32 s5, 0x1fff
	s_cselect_b32 s16, s64, 0x80
	s_cmpk_lg_i32 s14, 0x2000
	s_cselect_b32 s14, s16, 0x88
	s_add_u32 s16, s0, s14
	s_addc_u32 s17, s1, 0
	s_ashr_i32 s14, s7, 31
	s_lshr_b32 s14, s14, 20
	s_add_i32 s14, s7, s14
	s_and_b32 s14, s14, 0xf000
	s_sub_i32 s7, s7, s14
	s_sext_i32_i16 s14, s7
	s_lshr_b32 s14, s14, 15
	s_bfe_u32 s18, s14, 0x4000c
	s_add_i32 s18, s7, s18
	s_and_b32 s18, s18, 0xfff0
	s_bfe_u32 s14, s14, 0x80008
	s_sub_i32 s18, s7, s18
	s_add_i32 s14, s7, s14
	s_sext_i32_i16 s23, s18
	s_sext_i32_i16 s18, s14
	s_and_b32 s14, s14, 0xff00
	s_load_dwordx2 s[16:17], s[16:17], 0x0
	s_ashr_i32 s18, s18, 8
	s_sub_i32 s7, s7, s14
	s_sext_i32_i16 s14, s7
	s_add_i32 s18, s18, 16
	s_bfe_u32 s14, s14, 0x4001b
	s_and_b32 s52, s18, 0xffff
	s_add_i32 s7, s7, s14
	s_lshl_b64 s[18:19], s[52:53], 24
	s_waitcnt lgkmcnt(0)
	s_add_u32 s14, s16, s18
	s_sext_i32_i16 s7, s7
	s_addc_u32 s18, s17, s19
	v_mov_b32_e32 v1, v0
	s_lshl_b32 s16, s23, 7
	s_lshl_b32 s7, s7, 3
	v_ashrrev_i32_e32 v2, 3, v1
	s_ashr_i32 s17, s16, 31
	s_and_b32 s7, s7, 0xffffff80
	v_and_b32_e32 v2, -4, v2
	s_lshl_b64 s[16:17], s[16:17], 2
	v_add_u32_e32 v72, s7, v2
	s_add_u32 s16, s14, s16
	v_lshlrev_b32_e32 v1, 4, v1
	s_addc_u32 s17, s18, s17
	v_and_b32_e32 v2, 0x1f0, v1
	v_ashrrev_i32_e32 v73, 31, v72
	v_lshl_add_u64 v[74:75], s[16:17], 0, v[2:3]
	v_lshlrev_b64 v[36:37], 13, v[72:73]
	v_lshl_add_u64 v[92:93], v[74:75], 0, v[36:37]
	v_add_co_u32_e32 v84, vcc, s94, v92
	v_or_b32_e32 v36, 1, v72
	s_nop 0
	v_addc_co_u32_e32 v85, vcc, 0, v93, vcc
	v_add_co_u32_e32 v88, vcc, 0x82000, v92
	v_or_b32_e32 v76, 2, v72
	s_nop 0
	v_addc_co_u32_e32 v89, vcc, 0, v93, vcc
	v_or_b32_e32 v72, 3, v72
	v_add_co_u32_e32 v94, vcc, 0x84000, v92
	v_ashrrev_i32_e32 v37, 31, v36
	v_ashrrev_i32_e32 v77, 31, v76
	v_ashrrev_i32_e32 v73, 31, v72
	v_addc_co_u32_e32 v95, vcc, 0, v93, vcc
	v_lshlrev_b64 v[36:37], 13, v[36:37]
	v_lshlrev_b64 v[76:77], 13, v[76:77]
	v_lshlrev_b64 v[72:73], 13, v[72:73]
	v_add_co_u32_e32 v96, vcc, 0x86000, v92
	v_lshl_add_u64 v[40:41], v[74:75], 0, v[36:37]
	v_lshl_add_u64 v[76:77], v[74:75], 0, v[76:77]
	v_lshl_add_u64 v[78:79], v[74:75], 0, v[72:73]
	v_addc_co_u32_e32 v97, vcc, 0, v93, vcc
	global_load_dwordx4 v[36:39], v[92:93], off nt
	s_nop 0
	global_load_dwordx4 v[40:43], v[40:41], off nt
	s_nop 0
	global_load_dwordx4 v[72:75], v[76:77], off nt
	s_nop 0
	global_load_dwordx4 v[76:79], v[78:79], off nt
	s_nop 0
	global_load_dwordx4 v[84:87], v[84:85], off nt
	s_nop 0
	global_load_dwordx4 v[88:91], v[88:89], off nt
	s_nop 0
	global_load_dwordx4 v[92:95], v[94:95], off nt
	s_nop 0
	global_load_dwordx4 v[96:99], v[96:97], off nt

; DEVI int opaque_tid() { int t = threadIdx.x; asm volatile("" : "+v"(t)); return t; }
; DEVI void cvt8_load(const Params& p, int L, int t, CvtIn& in) {
;     const int which = t / 4096, r = t % 4096, le = L * 16 + r / 256, kt = (r % 256) / 16, nt = r % 16;
;     const float* src = (which == 2 ? p.w_down : (which == 0 ? p.w_gate : p.w_up)) + (size_t)le * 2048 * 2048;
;     const int tid = opaque_tid(), nq = tid & 31, kq0 = tid >> 5;
; #pragma unroll
;     for (int it = 0; it < 2; ++it)
; #pragma unroll
;         for (int kk = 0; kk < 4; ++kk) in.v[it * 4 + kk] = __builtin_nontemporal_load((const f32x4*)(src + (size_t)(kt * 128 + (kq0 + it * 16) * 4 + kk) * 2048 + nt * 128 + nq * 4));
; }
; DEVI void cvt8_stream3(const Params& p, int L, int t0, int step, int count, char* smem) {
;     if (count <= 0) return;
;     CvtIn a, b; cvt8_load(p, L, t0, a);
;     if (count > 1) cvt8_load(p, L, t0 + step, b);
.LBB0_784:
	s_and_b64 vcc, exec, s[16:17]
	s_cbranch_vccz .LBB0_801
	s_add_i32 s7, s6, 0x1f10
	s_and_b32 s4, s7, 0xfffff000
	s_add_i32 s5, s6, 0x2f0f
	s_cmpk_lt_u32 s5, 0x1fff
	s_cselect_b32 s5, s64, 0x80
	s_cmpk_lg_i32 s4, 0x2000
	s_cselect_b32 s4, s5, 0x88
	s_add_u32 s4, s0, s4
	s_addc_u32 s5, s1, 0
	s_ashr_i32 s14, s7, 31
	s_lshr_b32 s14, s14, 20
	s_add_i32 s14, s7, s14
	s_and_b32 s14, s14, 0xf000
	s_sub_i32 s7, s7, s14
	s_sext_i32_i16 s14, s7
	s_lshr_b32 s14, s14, 15
	s_bfe_u32 s16, s14, 0x4000c
	s_add_i32 s16, s7, s16
	s_and_b32 s16, s16, 0xfff0
	s_sub_i32 s16, s7, s16
	s_bfe_u32 s14, s14, 0x80008
	s_sext_i32_i16 s18, s16
	s_add_i32 s16, s7, s14
	s_sext_i32_i16 s14, s16
	s_and_b32 s16, s16, 0xff00
	s_sub_i32 s7, s7, s16
	s_load_dwordx2 s[4:5], s[4:5], 0x0
	s_sext_i32_i16 s16, s7
	s_lshr_b32 s14, s14, 8
	s_bfe_u32 s16, s16, 0x4001b
	s_add_i32 s7, s7, s16
	s_bfe_i64 s[16:17], s[14:15], 0x100000
	s_lshl_b64 s[16:17], s[16:17], 24
	s_sext_i32_i16 s7, s7
	s_waitcnt lgkmcnt(0)
	s_add_u32 s14, s4, s16
	v_mov_b32_e32 v1, v0
	s_addc_u32 s16, s5, s17
	s_lshl_b32 s4, s7, 3
	v_ashrrev_i32_e32 v2, 3, v1
	s_and_b32 s4, s4, 0xffffff80
	v_and_b32_e32 v2, -4, v2
	s_waitcnt vmcnt(2)
	v_add_u32_e32 v4, s4, v2
	s_lshl_b32 s4, s18, 7
	s_ashr_i32 s5, s4, 31
	s_lshl_b64 s[4:5], s[4:5], 2
	s_add_u32 s4, s14, s4
	v_lshlrev_b32_e32 v1, 4, v1
	s_addc_u32 s5, s16, s5
	v_and_b32_e32 v2, 0x1f0, v1
	v_ashrrev_i32_e32 v5, 31, v4
	v_lshl_add_u64 v[6:7], s[4:5], 0, v[2:3]
	s_waitcnt vmcnt(1)
	v_lshlrev_b64 v[8:9], 13, v[4:5]
	v_lshl_add_u64 v[12:13], v[6:7], 0, v[8:9]
	v_or_b32_e32 v8, 1, v4
	v_ashrrev_i32_e32 v9, 31, v8
	v_lshlrev_b64 v[8:9], 13, v[8:9]
	v_lshl_add_u64 v[8:9], v[6:7], 0, v[8:9]
	global_load_dwordx4 v[20:23], v[12:13], off nt
	global_load_dwordx4 v[24:27], v[8:9], off nt
	v_or_b32_e32 v8, 2, v4
	v_or_b32_e32 v4, 3, v4
	v_ashrrev_i32_e32 v9, 31, v8
	v_ashrrev_i32_e32 v5, 31, v4
	v_lshlrev_b64 v[8:9], 13, v[8:9]
	v_lshlrev_b64 v[4:5], 13, v[4:5]
	v_lshl_add_u64 v[8:9], v[6:7], 0, v[8:9]
	v_lshl_add_u64 v[4:5], v[6:7], 0, v[4:5]
	global_load_dwordx4 v[28:31], v[8:9], off nt
	global_load_dwordx4 v[32:35], v[4:5], off nt
	v_add_co_u32_e32 v4, vcc, s94, v12
	s_mov_b32 s19, 0x82000
	s_nop 0
	v_addc_co_u32_e32 v5, vcc, 0, v13, vcc
	v_add_co_u32_e32 v8, vcc, s19, v12
	s_mov_b32 s4, 0x84000
	s_nop 0
	v_addc_co_u32_e32 v9, vcc, 0, v13, vcc
	v_add_co_u32_e32 v14, vcc, s4, v12
	s_mov_b32 s4, 0x86000
	s_nop 0
	v_addc_co_u32_e32 v15, vcc, 0, v13, vcc
	s_add_i32 s7, s6, 0x1f30
	v_add_co_u32_e32 v16, vcc, s4, v12
	s_and_b32 s4, s7, 0xfffff000
	s_add_i32 s5, s6, 0x2f2f
	s_cmpk_lt_u32 s5, 0x1fff
	s_cselect_b32 s5, s64, 0x80
	s_cmpk_lg_i32 s4, 0x2000
	s_cselect_b32 s4, s5, 0x88
	s_add_u32 s4, s0, s4
	s_addc_u32 s5, s1, 0
	s_ashr_i32 s14, s7, 31
	s_lshr_b32 s14, s14, 20
	s_add_i32 s14, s7, s14
	s_and_b32 s14, s14, 0xf000
	s_sub_i32 s7, s7, s14
	s_sext_i32_i16 s14, s7
	s_lshr_b32 s14, s14, 15
	s_bfe_u32 s16, s14, 0x4000c
	s_add_i32 s16, s7, s16
	s_and_b32 s16, s16, 0xfff0
	s_sub_i32 s16, s7, s16
	s_bfe_u32 s14, s14, 0x80008
	s_sext_i32_i16 s18, s16
	s_add_i32 s16, s7, s14
	v_addc_co_u32_e32 v17, vcc, 0, v13, vcc
	s_sext_i32_i16 s14, s16
	s_and_b32 s16, s16, 0xff00
	global_load_dwordx4 v[4:7], v[4:5], off nt
	s_nop 0
	global_load_dwordx4 v[8:11], v[8:9], off nt
	s_nop 0
	global_load_dwordx4 v[12:15], v[14:15], off nt
	s_nop 0
	global_load_dwordx4 v[16:19], v[16:17], off nt
	s_sub_i32 s7, s7, s16
	s_load_dwordx2 s[4:5], s[4:5], 0x0
	s_sext_i32_i16 s16, s7
	s_lshr_b32 s14, s14, 8
	s_bfe_u32 s16, s16, 0x4001b
	s_add_i32 s7, s7, s16
	s_bfe_i64 s[16:17], s[14:15], 0x100000
	s_lshl_b64 s[16:17], s[16:17], 24
	s_sext_i32_i16 s7, s7
	s_waitcnt lgkmcnt(0)
	s_add_u32 s14, s4, s16
	v_mov_b32_e32 v1, v0
	s_addc_u32 s16, s5, s17
	s_lshl_b32 s4, s7, 3
	v_ashrrev_i32_e32 v2, 3, v1
	s_and_b32 s4, s4, 0xffffff80
	v_and_b32_e32 v2, -4, v2
	v_add_u32_e32 v44, s4, v2
	s_lshl_b32 s4, s18, 7
	s_ashr_i32 s5, s4, 31
	s_lshl_b64 s[4:5], s[4:5], 2
	s_add_u32 s4, s14, s4
	v_lshlrev_b32_e32 v1, 4, v1
	s_addc_u32 s5, s16, s5
	v_and_b32_e32 v2, 0x1f0, v1
	v_ashrrev_i32_e32 v45, 31, v44
	v_lshl_add_u64 v[46:47], s[4:5], 0, v[2:3]
	v_lshlrev_b64 v[36:37], 13, v[44:45]
	v_lshl_add_u64 v[48:49], v[46:47], 0, v[36:37]
	v_or_b32_e32 v36, 1, v44
	v_or_b32_e32 v50, 2, v44
	v_or_b32_e32 v44, 3, v44
	v_ashrrev_i32_e32 v37, 31, v36
	v_ashrrev_i32_e32 v51, 31, v50
	v_ashrrev_i32_e32 v45, 31, v44
	v_lshlrev_b64 v[36:37], 13, v[36:37]
	v_lshlrev_b64 v[50:51], 13, v[50:51]
	v_lshlrev_b64 v[44:45], 13, v[44:45]
	v_lshl_add_u64 v[40:41], v[46:47], 0, v[36:37]
	v_lshl_add_u64 v[50:51], v[46:47], 0, v[50:51]
	v_lshl_add_u64 v[44:45], v[46:47], 0, v[44:45]
	global_load_dwordx4 v[36:39], v[48:49], off nt
	s_nop 0
	global_load_dwordx4 v[40:43], v[40:41], off nt
	s_nop 0
	global_load_dwordx4 v[72:75], v[50:51], off nt
	global_load_dwordx4 v[76:79], v[44:45], off nt
	v_add_co_u32_e32 v44, vcc, s94, v48
	s_mov_b32 s4, 0
	s_nop 0
	v_addc_co_u32_e32 v45, vcc, 0, v49, vcc
	v_add_co_u32_e32 v46, vcc, s19, v48
	s_add_i32 s5, s6, 0x2f4f
	s_nop 0
	v_addc_co_u32_e32 v47, vcc, 0, v49, vcc
	global_load_dwordx4 v[84:87], v[44:45], off nt
	global_load_dwordx4 v[88:91], v[46:47], off nt
	v_add_co_u32_e32 v44, vcc, 0x84000, v48
	s_nop 1
	v_addc_co_u32_e32 v45, vcc, 0, v49, vcc
	v_add_co_u32_e32 v46, vcc, 0x86000, v48
	s_nop 1
	v_addc_co_u32_e32 v47, vcc, 0, v49, vcc
	global_load_dwordx4 v[92:95], v[44:45], off nt
	global_load_dwordx4 v[96:99], v[46:47], off nt
	s_branch .LBB0_787
; DEVI int opaque_tid() { int t = threadIdx.x; asm volatile("" : "+v"(t)); return t; }
; DEVI unsigned cvt4_fp8(float a, float b, float c, float d) { int w = 0; w = __builtin_amdgcn_cvt_pk_fp8_f32(a, b, w, false); w = __builtin_amdgcn_cvt_pk_fp8_f32(c, d, w, true); return (unsigned)w; }
; DEVI void cvt8_finish(const Params& p, int L, int t, const CvtIn& in, char* smem) {
;     const int which = t / 4096, r = t % 4096, le = L * 16 + r / 256, kt = (r % 256) / 16, nt = r % 16;
;     unsigned char* dst = (which == 2) ? (unsigned char*)(p.ws + WS_WDN) + (size_t)le * 2048 * 2048 + (size_t)(nt * 128) * 2048
;                                       : (unsigned char*)(p.ws + WS_WGU) + (size_t)le * 4096 * 2048 + (size_t)(nt * 256 + which * 128) * 2048;
;     unsigned char* T = (unsigned char*)smem;
;     const int tid = opaque_tid(), nq = tid & 31, kq0 = tid >> 5;
; #pragma unroll
;     for (int it = 0; it < 2; ++it) { const int kq = kq0 + it * 16;
; #pragma unroll
;         for (int j = 0; j < 4; ++j) *(unsigned*)(T + (nq * 4 + j) * 144 + kq * 4) =
;             cvt4_fp8(in.v[it * 4][j] * W8_SCALE, in.v[it * 4 + 1][j] * W8_SCALE, in.v[it * 4 + 2][j] * W8_SCALE, in.v[it * 4 + 3][j] * W8_SCALE); }
;     __syncthreads();
; #pragma unroll
;     for (int i = 0; i < 2; ++i) { const int nl = (tid >> 3) + 64 * i, kc = (tid & 7) * 16;
;         *(u32x4*)(dst + (size_t)nl * 2048 + kt * 128 + kc) = *(const u32x4*)(T + nl * 144 + kc); }
;     __syncthreads();
; }
; DEVI void cvt8_stream3(const Params& p, int L, int t0, int step, int count, char* smem) {
;     ...
; #pragma nounroll
;     for (int i = 0; i < count; ++i) { CvtIn c;
;         if (i + 2 < count) cvt8_load(p, L, t0 + (i + 2) * step, c);
;         cvt8_finish(p, L, t0 + i * step, a, smem);
;         a = b; b = c; }
.LBB0_786:
	v_mul_f32_e32 v20, 0x42800000, v20
	v_mul_f32_e32 v24, 0x42800000, v24
	v_mov_b32_e32 v101, v3
	v_cvt_pk_fp8_f32 v101, v20, v24
	v_mul_f32_e32 v24, 0x42800000, v28
	v_mul_f32_e32 v28, 0x42800000, v32
	v_mov_b32_e32 v1, v0
	v_cvt_pk_fp8_f32 v101, v24, v28 op_sel:[0,0,1]
	v_mul_f32_e32 v21, 0x42800000, v21
	v_mul_f32_e32 v24, 0x42800000, v25
	v_mov_b32_e32 v25, v3
	v_cvt_pk_fp8_f32 v25, v21, v24
	v_lshlrev_b32_e32 v2, 2, v1
	v_and_b32_e32 v2, 0x7c, v2
	v_ashrrev_i32_e32 v100, 3, v1
	v_and_b32_e32 v20, -4, v100
	v_mul_u32_u24_e32 v2, 0x90, v2
	v_add3_u32 v2, 0, v20, v2
	v_mul_f32_e32 v20, 0x42800000, v29
	v_mul_f32_e32 v21, 0x42800000, v33
	v_cvt_pk_fp8_f32 v25, v20, v21 op_sel:[0,0,1]
	v_mul_f32_e32 v20, 0x42800000, v22
	v_mul_f32_e32 v21, 0x42800000, v26
	v_mov_b32_e32 v26, v3
	v_cvt_pk_fp8_f32 v26, v20, v21
	v_mul_f32_e32 v20, 0x42800000, v23
	v_mul_f32_e32 v21, 0x42800000, v27
	v_mov_b32_e32 v23, v3
	v_cvt_pk_fp8_f32 v23, v20, v21
	v_mul_f32_e32 v20, 0x42800000, v31
	v_mul_f32_e32 v21, 0x42800000, v35
	v_mul_f32_e32 v4, 0x42800000, v4
	v_cvt_pk_fp8_f32 v23, v20, v21 op_sel:[0,0,1]
	v_mul_f32_e32 v8, 0x42800000, v8
	v_mov_b32_e32 v20, v3
	v_cvt_pk_fp8_f32 v20, v4, v8
	v_mul_f32_e32 v4, 0x42800000, v5
	v_mul_f32_e32 v5, 0x42800000, v9
	v_mov_b32_e32 v8, v3
	v_cvt_pk_fp8_f32 v8, v4, v5
	s_lshl_b32 s14, s14, 8
	v_mul_f32_e32 v4, 0x42800000, v13
	v_mul_f32_e32 v5, 0x42800000, v17
	s_sub_i32 s7, s7, s14
	v_cvt_pk_fp8_f32 v8, v4, v5 op_sel:[0,0,1]
	v_mul_f32_e32 v4, 0x42800000, v6
	v_mul_f32_e32 v5, 0x42800000, v10
	v_mov_b32_e32 v10, v3
	s_sext_i32_i16 s14, s7
	v_cvt_pk_fp8_f32 v10, v4, v5
	v_mul_f32_e32 v4, 0x42800000, v7
	v_mul_f32_e32 v5, 0x42800000, v11
	v_mov_b32_e32 v7, v3
	s_bfe_u32 s14, s14, 0x4001b
	v_mul_f32_e32 v12, 0x42800000, v12
	v_mul_f32_e32 v16, 0x42800000, v16
	v_cvt_pk_fp8_f32 v7, v4, v5
	s_add_i32 s7, s7, s14
	v_cvt_pk_fp8_f32 v20, v12, v16 op_sel:[0,0,1]
	s_sext_i32_i16 s7, s7
	v_mul_f32_e32 v22, 0x42800000, v30
	v_mul_f32_e32 v24, 0x42800000, v34
	v_mul_f32_e32 v6, 0x42800000, v14
	v_mul_f32_e32 v9, 0x42800000, v18
	v_cvt_pk_fp8_f32 v26, v22, v24 op_sel:[0,0,1]
	v_cvt_pk_fp8_f32 v10, v6, v9 op_sel:[0,0,1]
	v_mul_f32_e32 v4, 0x42800000, v15
	v_mul_f32_e32 v5, 0x42800000, v19
	s_lshl_b32 s7, s7, 3
	v_cvt_pk_fp8_f32 v7, v4, v5 op_sel:[0,0,1]
	v_lshlrev_b32_e32 v1, 4, v1
	s_and_b32 s7, s7, 0xffffff80
	ds_write2_b32 v2, v101, v20 offset1:16
	ds_write2_b32 v2, v25, v8 offset0:36 offset1:52
	ds_write2_b32 v2, v26, v10 offset0:72 offset1:88
	ds_write2_b32 v2, v23, v7 offset0:108 offset1:124
	v_and_b32_e32 v2, 0x70, v1
	s_ashr_i32 s14, s7, 31
	v_mul_lo_u32 v1, v100, s91
	s_add_u32 s16, s16, s7
	v_add3_u32 v1, 0, v2, v1
	s_waitcnt lgkmcnt(0)
	s_barrier
	s_addc_u32 s17, s17, s14
	ds_read_b128 v[4:7], v1
	v_ashrrev_i32_e32 v101, 31, v100
	v_lshl_add_u64 v[8:9], s[16:17], 0, v[2:3]
	v_lshlrev_b64 v[10:11], 11, v[100:101]
	v_lshl_add_u64 v[12:13], v[8:9], 0, v[10:11]
	ds_read_b128 v[8:11], v1 offset:9216
	s_waitcnt lgkmcnt(1)
	global_store_dwordx4 v[12:13], v[4:7], off
	s_add_i32 s4, s4, 1
	s_add_i32 s5, s5, 32
	v_add_co_u32_e32 v4, vcc, 0x20000, v12
	v_mov_b64_e32 v[20:21], v[80:81]
	s_nop 0
	v_addc_co_u32_e32 v5, vcc, 0, v13, vcc
	s_waitcnt lgkmcnt(0)
	global_store_dwordx4 v[4:5], v[8:11], off
	v_mov_b64_e32 v[24:25], v[68:69]
	v_mov_b64_e32 v[28:29], v[64:65]
	v_mov_b64_e32 v[32:33], v[60:61]
	v_mov_b64_e32 v[4:5], v[56:57]
	v_mov_b64_e32 v[8:9], v[52:53]
	v_mov_b64_e32 v[12:13], v[48:49]
	v_mov_b64_e32 v[16:17], v[44:45]
	s_cmp_lg_u32 s4, 56
	v_mov_b64_e32 v[22:23], v[82:83]
	v_mov_b64_e32 v[26:27], v[70:71]
	v_mov_b64_e32 v[30:31], v[66:67]
	v_mov_b64_e32 v[34:35], v[62:63]
	v_mov_b64_e32 v[6:7], v[58:59]
	v_mov_b64_e32 v[10:11], v[54:55]
	v_mov_b64_e32 v[14:15], v[50:51]
	v_mov_b64_e32 v[18:19], v[46:47]
	s_barrier
	s_cbranch_scc0 .LBB0_793
; DEVI int opaque_tid() { int t = threadIdx.x; asm volatile("" : "+v"(t)); return t; }
; DEVI void cvt8_load(const Params& p, int L, int t, CvtIn& in) {
;     const int which = t / 4096, r = t % 4096, le = L * 16 + r / 256, kt = (r % 256) / 16, nt = r % 16;
;     const float* src = (which == 2 ? p.w_down : (which == 0 ? p.w_gate : p.w_up)) + (size_t)le * 2048 * 2048;
;     const int tid = opaque_tid(), nq = tid & 31, kq0 = tid >> 5;
; #pragma unroll
;     for (int it = 0; it < 2; ++it)
; #pragma unroll
;         for (int kk = 0; kk < 4; ++kk) in.v[it * 4 + kk] = __builtin_nontemporal_load((const f32x4*)(src + (size_t)(kt * 128 + (kq0 + it * 16) * 4 + kk) * 2048 + nt * 128 + nq * 4));
; }
; DEVI void cvt8_stream3(const Params& p, int L, int t0, int step, int count, char* smem) {
;     ...
; #pragma nounroll
;     for (int i = 0; i < count; ++i) { CvtIn c;
;         if (i + 2 < count) cvt8_load(p, L, t0 + (i + 2) * step, c);
;         cvt8_finish(p, L, t0 + i * step, a, smem);
;         a = b; b = c; }
.LBB0_787:
	s_waitcnt vmcnt(0)
	v_mov_b64_e32 v[44:45], v[96:97]
	v_mov_b64_e32 v[48:49], v[92:93]
	v_mov_b64_e32 v[52:53], v[88:89]
	v_mov_b64_e32 v[56:57], v[84:85]
	v_mov_b64_e32 v[60:61], v[76:77]
	v_mov_b64_e32 v[64:65], v[72:73]
	v_mov_b64_e32 v[70:71], v[42:43]
	v_mov_b64_e32 v[82:83], v[38:39]
	v_mov_b64_e32 v[46:47], v[98:99]
	v_mov_b64_e32 v[50:51], v[94:95]
	v_mov_b64_e32 v[54:55], v[90:91]
	v_mov_b64_e32 v[58:59], v[86:87]
	v_mov_b64_e32 v[62:63], v[78:79]
	v_mov_b64_e32 v[66:67], v[74:75]
	v_mov_b64_e32 v[68:69], v[40:41]
	s_cmp_gt_u32 s4, 53
	v_mov_b64_e32 v[80:81], v[36:37]
	s_cbranch_scc1 .LBB0_789
	s_add_i32 s7, s5, 0xfffff001
	s_and_b32 s14, s7, 0xfffff000
	s_cmpk_lt_u32 s5, 0x1fff
	s_cselect_b32 s16, s64, 0x80
	s_cmpk_lg_i32 s14, 0x2000
	s_cselect_b32 s14, s16, 0x88
	s_add_u32 s16, s0, s14
	s_addc_u32 s17, s1, 0
	s_ashr_i32 s14, s7, 31
	s_lshr_b32 s14, s14, 20
	s_add_i32 s14, s7, s14
	s_and_b32 s14, s14, 0xf000
	s_sub_i32 s7, s7, s14
	s_sext_i32_i16 s14, s7
	s_lshr_b32 s14, s14, 15
	s_bfe_u32 s18, s14, 0x4000c
	s_add_i32 s18, s7, s18
	s_and_b32 s18, s18, 0xfff0
	s_sub_i32 s18, s7, s18
	s_bfe_u32 s14, s14, 0x80008
	s_sext_i32_i16 s23, s18
	s_add_i32 s18, s7, s14
	s_sext_i32_i16 s14, s18
	s_and_b32 s18, s18, 0xff00
	s_sub_i32 s7, s7, s18
	s_load_dwordx2 s[16:17], s[16:17], 0x0
	s_sext_i32_i16 s18, s7
	s_lshr_b32 s14, s14, 8
	s_bfe_u32 s18, s18, 0x4001b
	s_add_i32 s7, s7, s18
	s_bfe_i64 s[18:19], s[14:15], 0x100000
	s_lshl_b64 s[18:19], s[18:19], 24
	s_waitcnt lgkmcnt(0)
	s_add_u32 s14, s16, s18
	s_sext_i32_i16 s7, s7
	s_addc_u32 s18, s17, s19
	v_mov_b32_e32 v1, v0
	s_lshl_b32 s16, s23, 7
	s_lshl_b32 s7, s7, 3
	v_ashrrev_i32_e32 v2, 3, v1
	s_ashr_i32 s17, s16, 31
	s_and_b32 s7, s7, 0xffffff80
	v_and_b32_e32 v2, -4, v2
	s_lshl_b64 s[16:17], s[16:17], 2
	v_add_u32_e32 v72, s7, v2
	s_add_u32 s16, s14, s16
	v_lshlrev_b32_e32 v1, 4, v1
	s_addc_u32 s17, s18, s17
	v_and_b32_e32 v2, 0x1f0, v1
	v_ashrrev_i32_e32 v73, 31, v72
	v_lshl_add_u64 v[74:75], s[16:17], 0, v[2:3]
	v_lshlrev_b64 v[36:37], 13, v[72:73]
	v_lshl_add_u64 v[92:93], v[74:75], 0, v[36:37]
	v_add_co_u32_e32 v84, vcc, s94, v92
	v_or_b32_e32 v36, 1, v72
	s_nop 0
	v_addc_co_u32_e32 v85, vcc, 0, v93, vcc
	v_add_co_u32_e32 v88, vcc, 0x82000, v92
	v_or_b32_e32 v76, 2, v72
	s_nop 0
	v_addc_co_u32_e32 v89, vcc, 0, v93, vcc
	v_or_b32_e32 v72, 3, v72
	v_add_co_u32_e32 v94, vcc, 0x84000, v92
	v_ashrrev_i32_e32 v37, 31, v36
	v_ashrrev_i32_e32 v77, 31, v76
	v_ashrrev_i32_e32 v73, 31, v72
	v_addc_co_u32_e32 v95, vcc, 0, v93, vcc
	v_lshlrev_b64 v[36:37], 13, v[36:37]
	v_lshlrev_b64 v[76:77], 13, v[76:77]
	v_lshlrev_b64 v[72:73], 13, v[72:73]
	v_add_co_u32_e32 v96, vcc, 0x86000, v92
	v_lshl_add_u64 v[40:41], v[74:75], 0, v[36:37]
	v_lshl_add_u64 v[76:77], v[74:75], 0, v[76:77]
	v_lshl_add_u64 v[78:79], v[74:75], 0, v[72:73]
	v_addc_co_u32_e32 v97, vcc, 0, v93, vcc
	global_load_dwordx4 v[36:39], v[92:93], off nt
	s_nop 0
	global_load_dwordx4 v[40:43], v[40:41], off nt
	s_nop 0
	global_load_dwordx4 v[72:75], v[76:77], off nt
	s_nop 0
	global_load_dwordx4 v[76:79], v[78:79], off nt
	s_nop 0
	global_load_dwordx4 v[84:87], v[84:85], off nt
	s_nop 0
	global_load_dwordx4 v[88:91], v[88:89], off nt
	s_nop 0
	global_load_dwordx4 v[92:95], v[94:95], off nt
	s_nop 0
	global_load_dwordx4 v[96:99], v[96:97], off nt

; DEVI int opaque_tid() { int t = threadIdx.x; asm volatile("" : "+v"(t)); return t; }
; DEVI void cvt8_load(const Params& p, int L, int t, CvtIn& in) {
;     const int which = t / 4096, r = t % 4096, le = L * 16 + r / 256, kt = (r % 256) / 16, nt = r % 16;
;     const float* src = (which == 2 ? p.w_down : (which == 0 ? p.w_gate : p.w_up)) + (size_t)le * 2048 * 2048;
;     const int tid = opaque_tid(), nq = tid & 31, kq0 = tid >> 5;
; #pragma unroll
;     for (int it = 0; it < 2; ++it)
; #pragma unroll
;         for (int kk = 0; kk < 4; ++kk) in.v[it * 4 + kk] = __builtin_nontemporal_load((const f32x4*)(src + (size_t)(kt * 128 + (kq0 + it * 16) * 4 + kk) * 2048 + nt * 128 + nq * 4));
; }
; DEVI void cvt8_stream3(const Params& p, int L, int t0, int step, int count, char* smem) {
;     if (count <= 0) return;
;     CvtIn a, b; cvt8_load(p, L, t0, a);
;     if (count > 1) cvt8_load(p, L, t0 + step, b);
.LBB0_793:
	s_add_i32 s7, s6, 0x17d0
	s_and_b32 s4, s7, 0xfffff000
	s_add_i32 s5, s6, 0x27cf
	s_cmpk_lt_u32 s5, 0x1fff
	s_cselect_b32 s5, s64, 0x80
	s_cmpk_lg_i32 s4, 0x2000
	s_cselect_b32 s4, s5, 0x88
	s_add_u32 s4, s0, s4
	s_addc_u32 s5, s1, 0
	s_ashr_i32 s14, s7, 31
	s_lshr_b32 s14, s14, 20
	s_add_i32 s14, s7, s14
	s_and_b32 s14, s14, 0xf000
	s_sub_i32 s7, s7, s14
	s_sext_i32_i16 s14, s7
	s_lshr_b32 s14, s14, 15
	s_bfe_u32 s16, s14, 0x4000c
	s_add_i32 s16, s7, s16
	s_and_b32 s16, s16, 0xfff0
	s_bfe_u32 s14, s14, 0x80008
	s_sub_i32 s16, s7, s16
	s_add_i32 s14, s7, s14
	s_sext_i32_i16 s18, s16
	s_sext_i32_i16 s16, s14
	s_and_b32 s14, s14, 0xff00
	s_load_dwordx2 s[4:5], s[4:5], 0x0
	s_ashr_i32 s16, s16, 8
	s_sub_i32 s7, s7, s14
	s_sext_i32_i16 s14, s7
	s_add_i32 s16, s16, 16
	s_bfe_u32 s14, s14, 0x4001b
	s_and_b32 s52, s16, 0xffff
	s_add_i32 s7, s7, s14
	s_lshl_b64 s[16:17], s[52:53], 24
	s_sext_i32_i16 s7, s7
	s_waitcnt lgkmcnt(0)
	s_add_u32 s14, s4, s16
	v_mov_b32_e32 v1, v0
	s_addc_u32 s16, s5, s17
	s_lshl_b32 s4, s7, 3
	v_ashrrev_i32_e32 v2, 3, v1
	s_and_b32 s4, s4, 0xffffff80
	v_and_b32_e32 v2, -4, v2
	v_add_u32_e32 v4, s4, v2
	s_lshl_b32 s4, s18, 7
	s_ashr_i32 s5, s4, 31
	s_lshl_b64 s[4:5], s[4:5], 2
	s_add_u32 s4, s14, s4
	v_lshlrev_b32_e32 v1, 4, v1
	s_addc_u32 s5, s16, s5
	v_and_b32_e32 v2, 0x1f0, v1
	v_ashrrev_i32_e32 v5, 31, v4
	v_lshl_add_u64 v[6:7], s[4:5], 0, v[2:3]
	v_lshlrev_b64 v[8:9], 13, v[4:5]
	v_lshl_add_u64 v[12:13], v[6:7], 0, v[8:9]
	v_or_b32_e32 v8, 1, v4
	v_ashrrev_i32_e32 v9, 31, v8
	v_lshlrev_b64 v[8:9], 13, v[8:9]
	v_lshl_add_u64 v[8:9], v[6:7], 0, v[8:9]
	global_load_dwordx4 v[20:23], v[12:13], off nt
	global_load_dwordx4 v[24:27], v[8:9], off nt
	v_or_b32_e32 v8, 2, v4
	v_or_b32_e32 v4, 3, v4
	v_ashrrev_i32_e32 v9, 31, v8
	v_ashrrev_i32_e32 v5, 31, v4
	v_lshlrev_b64 v[8:9], 13, v[8:9]
	v_lshlrev_b64 v[4:5], 13, v[4:5]
	v_lshl_add_u64 v[8:9], v[6:7], 0, v[8:9]
	v_lshl_add_u64 v[4:5], v[6:7], 0, v[4:5]
	global_load_dwordx4 v[28:31], v[8:9], off nt
	global_load_dwordx4 v[32:35], v[4:5], off nt
	v_add_co_u32_e32 v4, vcc, s94, v12
	s_mov_b32 s4, 0x82000
	s_nop 0
	v_addc_co_u32_e32 v5, vcc, 0, v13, vcc
	v_add_co_u32_e32 v8, vcc, s4, v12
	s_mov_b32 s4, 0x84000
	s_nop 0
	v_addc_co_u32_e32 v9, vcc, 0, v13, vcc
	v_add_co_u32_e32 v14, vcc, s4, v12
	s_mov_b32 s4, 0x86000
	s_nop 0
	v_addc_co_u32_e32 v15, vcc, 0, v13, vcc
	s_add_i32 s7, s6, 0x17f0
	v_add_co_u32_e32 v16, vcc, s4, v12
	s_and_b32 s4, s7, 0xfffff000
	s_add_i32 s5, s6, 0x27ef
	s_cmpk_lt_u32 s5, 0x1fff
	s_cselect_b32 s5, s64, 0x80
	s_cmpk_lg_i32 s4, 0x2000
	s_cselect_b32 s4, s5, 0x88
	s_add_u32 s4, s0, s4
	s_addc_u32 s5, s1, 0
	s_ashr_i32 s14, s7, 31
	s_lshr_b32 s14, s14, 20
	s_add_i32 s14, s7, s14
	s_and_b32 s14, s14, 0xf000
	s_sub_i32 s7, s7, s14
	s_sext_i32_i16 s14, s7
	s_lshr_b32 s14, s14, 15
	s_bfe_u32 s16, s14, 0x4000c
	s_add_i32 s16, s7, s16
	s_and_b32 s16, s16, 0xfff0
	s_bfe_u32 s14, s14, 0x80008
	v_addc_co_u32_e32 v17, vcc, 0, v13, vcc
	s_sub_i32 s16, s7, s16
	s_add_i32 s14, s7, s14
	global_load_dwordx4 v[4:7], v[4:5], off nt
	s_nop 0
	global_load_dwordx4 v[8:11], v[8:9], off nt
	s_nop 0
	global_load_dwordx4 v[12:15], v[14:15], off nt
	s_nop 0
	global_load_dwordx4 v[16:19], v[16:17], off nt
	s_sext_i32_i16 s18, s16
	s_sext_i32_i16 s16, s14
	s_and_b32 s14, s14, 0xff00
	s_load_dwordx2 s[4:5], s[4:5], 0x0
	s_ashr_i32 s16, s16, 8
	s_sub_i32 s7, s7, s14
	s_sext_i32_i16 s14, s7
	s_add_i32 s16, s16, 16
	s_bfe_u32 s14, s14, 0x4001b
	s_and_b32 s52, s16, 0xffff
	s_add_i32 s7, s7, s14
	s_lshl_b64 s[16:17], s[52:53], 24
	s_sext_i32_i16 s7, s7
	s_waitcnt lgkmcnt(0)
	s_add_u32 s14, s4, s16
	v_mov_b32_e32 v1, v0
	s_addc_u32 s16, s5, s17
	s_lshl_b32 s4, s7, 3
	v_ashrrev_i32_e32 v2, 3, v1
	s_and_b32 s4, s4, 0xffffff80
	v_and_b32_e32 v2, -4, v2
	v_add_u32_e32 v44, s4, v2
	s_lshl_b32 s4, s18, 7
	s_ashr_i32 s5, s4, 31
	s_lshl_b64 s[4:5], s[4:5], 2
	s_add_u32 s4, s14, s4
	v_lshlrev_b32_e32 v1, 4, v1
	s_addc_u32 s5, s16, s5
	v_and_b32_e32 v2, 0x1f0, v1
	v_ashrrev_i32_e32 v45, 31, v44
	v_lshl_add_u64 v[46:47], s[4:5], 0, v[2:3]
	s_waitcnt vmcnt(17)
	v_lshlrev_b64 v[36:37], 13, v[44:45]
	v_lshl_add_u64 v[48:49], v[46:47], 0, v[36:37]
	v_or_b32_e32 v36, 1, v44
	v_or_b32_e32 v50, 2, v44
	v_or_b32_e32 v44, 3, v44
	v_ashrrev_i32_e32 v37, 31, v36
	v_ashrrev_i32_e32 v51, 31, v50
	v_ashrrev_i32_e32 v45, 31, v44
	v_lshlrev_b64 v[36:37], 13, v[36:37]
	v_lshlrev_b64 v[50:51], 13, v[50:51]
	v_lshlrev_b64 v[44:45], 13, v[44:45]
	s_waitcnt vmcnt(16)
	v_lshl_add_u64 v[40:41], v[46:47], 0, v[36:37]
	v_lshl_add_u64 v[50:51], v[46:47], 0, v[50:51]
	v_lshl_add_u64 v[44:45], v[46:47], 0, v[44:45]
	global_load_dwordx4 v[36:39], v[48:49], off nt
	s_nop 0
	global_load_dwordx4 v[40:43], v[40:41], off nt
	s_nop 0
	global_load_dwordx4 v[72:75], v[50:51], off nt
	global_load_dwordx4 v[76:79], v[44:45], off nt
	v_add_co_u32_e32 v44, vcc, s94, v48
	s_mov_b32 s4, 0
	s_nop 0
	v_addc_co_u32_e32 v45, vcc, 0, v49, vcc
	v_add_co_u32_e32 v46, vcc, 0x82000, v48
	s_add_i32 s5, s6, 0x280f
	s_nop 0
	v_addc_co_u32_e32 v47, vcc, 0, v49, vcc
	global_load_dwordx4 v[84:87], v[44:45], off nt
	global_load_dwordx4 v[88:91], v[46:47], off nt
	v_add_co_u32_e32 v44, vcc, 0x84000, v48
	s_nop 1
	v_addc_co_u32_e32 v45, vcc, 0, v49, vcc
	v_add_co_u32_e32 v46, vcc, 0x86000, v48
	s_nop 1
	v_addc_co_u32_e32 v47, vcc, 0, v49, vcc
	global_load_dwordx4 v[92:95], v[44:45], off nt
	global_load_dwordx4 v[96:99], v[46:47], off nt
	s_branch .LBB0_795

; DEVI int opaque_tid() { int t = threadIdx.x; asm volatile("" : "+v"(t)); return t; }
; DEVI unsigned cvt4_fp8(float a, float b, float c, float d) { int w = 0; w = __builtin_amdgcn_cvt_pk_fp8_f32(a, b, w, false); w = __builtin_amdgcn_cvt_pk_fp8_f32(c, d, w, true); return (unsigned)w; }
; DEVI void cvt8_finish(const Params& p, int L, int t, const CvtIn& in, char* smem) {
;     const int which = t / 4096, r = t % 4096, le = L * 16 + r / 256, kt = (r % 256) / 16, nt = r % 16;
;     unsigned char* dst = (which == 2) ? (unsigned char*)(p.ws + WS_WDN) + (size_t)le * 2048 * 2048 + (size_t)(nt * 128) * 2048
;                                       : (unsigned char*)(p.ws + WS_WGU) + (size_t)le * 4096 * 2048 + (size_t)(nt * 256 + which * 128) * 2048;
;     unsigned char* T = (unsigned char*)smem;
;     const int tid = opaque_tid(), nq = tid & 31, kq0 = tid >> 5;
; #pragma unroll
;     for (int it = 0; it < 2; ++it) { const int kq = kq0 + it * 16;
; #pragma unroll
;         for (int j = 0; j < 4; ++j) *(unsigned*)(T + (nq * 4 + j) * 144 + kq * 4) =
;             cvt4_fp8(in.v[it * 4][j] * W8_SCALE, in.v[it * 4 + 1][j] * W8_SCALE, in.v[it * 4 + 2][j] * W8_SCALE, in.v[it * 4 + 3][j] * W8_SCALE); }
;     __syncthreads();
; #pragma unroll
;     for (int i = 0; i < 2; ++i) { const int nl = (tid >> 3) + 64 * i, kc = (tid & 7) * 16;
;         *(u32x4*)(dst + (size_t)nl * 2048 + kt * 128 + kc) = *(const u32x4*)(T + nl * 144 + kc); }
;     __syncthreads();
; }
; DEVI void cvt8_stream3(const Params& p, int L, int t0, int step, int count, char* smem) {
;     ...
; #pragma nounroll
;     for (int i = 0; i < count; ++i) { CvtIn c;
;         if (i + 2 < count) cvt8_load(p, L, t0 + (i + 2) * step, c);
;         cvt8_finish(p, L, t0 + i * step, a, smem);
;         a = b; b = c; }
.LBB0_1167:
	v_mul_f32_e32 v12, 0x42800000, v12
	v_mul_f32_e32 v16, 0x42800000, v16
	v_mov_b32_e32 v101, v3
	v_cvt_pk_fp8_f32 v101, v12, v16
	v_mul_f32_e32 v16, 0x42800000, v20
	v_mul_f32_e32 v20, 0x42800000, v24
	v_mov_b32_e32 v1, v0
	v_cvt_pk_fp8_f32 v101, v16, v20 op_sel:[0,0,1]
	v_mul_f32_e32 v13, 0x42800000, v13
	v_mul_f32_e32 v16, 0x42800000, v17
	v_mov_b32_e32 v17, v3
	v_cvt_pk_fp8_f32 v17, v13, v16
	v_lshlrev_b32_e32 v2, 2, v1
	v_and_b32_e32 v2, 0x7c, v2
	v_ashrrev_i32_e32 v100, 3, v1
	v_and_b32_e32 v12, -4, v100
	v_mul_u32_u24_e32 v2, 0x90, v2
	v_add3_u32 v2, 0, v12, v2
	v_mul_f32_e32 v12, 0x42800000, v21
	v_mul_f32_e32 v13, 0x42800000, v25
	v_cvt_pk_fp8_f32 v17, v12, v13 op_sel:[0,0,1]
	v_mul_f32_e32 v12, 0x42800000, v14
	v_mul_f32_e32 v13, 0x42800000, v18
	v_mov_b32_e32 v18, v3
	v_cvt_pk_fp8_f32 v18, v12, v13
	v_mul_f32_e32 v14, 0x42800000, v22
	v_mul_f32_e32 v16, 0x42800000, v26
	v_mul_f32_e32 v4, 0x42800000, v4
	v_cvt_pk_fp8_f32 v18, v14, v16 op_sel:[0,0,1]
	v_mul_f32_e32 v8, 0x42800000, v8
	v_mov_b32_e32 v14, v3
	v_cvt_pk_fp8_f32 v14, v4, v8
	v_mul_f32_e32 v4, 0x42800000, v5
	v_mul_f32_e32 v5, 0x42800000, v9
	v_mov_b32_e32 v8, v3
	v_cvt_pk_fp8_f32 v8, v4, v5
	v_mul_f32_e32 v12, 0x42800000, v15
	v_mul_f32_e32 v13, 0x42800000, v19
	v_mov_b32_e32 v15, v3
	s_lshr_b32 s15, s15, 8
	v_cvt_pk_fp8_f32 v15, v12, v13
	s_lshl_b32 s15, s15, 8
	v_mul_f32_e32 v4, 0x42800000, v29
	v_mul_f32_e32 v5, 0x42800000, v33
	s_sub_i32 s14, s14, s15
	v_cvt_pk_fp8_f32 v8, v4, v5 op_sel:[0,0,1]
	v_mul_f32_e32 v4, 0x42800000, v6
	v_mul_f32_e32 v5, 0x42800000, v10
	v_mov_b32_e32 v10, v3
	s_sext_i32_i16 s15, s14
	v_mul_f32_e32 v12, 0x42800000, v23
	v_mul_f32_e32 v13, 0x42800000, v27
	v_cvt_pk_fp8_f32 v10, v4, v5
	v_mul_f32_e32 v4, 0x42800000, v7
	v_mul_f32_e32 v5, 0x42800000, v11
	v_mov_b32_e32 v7, v3
	s_bfe_u32 s15, s15, 0x4001b
	v_cvt_pk_fp8_f32 v15, v12, v13 op_sel:[0,0,1]
	v_mul_f32_e32 v12, 0x42800000, v28
	v_mul_f32_e32 v13, 0x42800000, v32
	v_cvt_pk_fp8_f32 v7, v4, v5
	s_add_i32 s14, s14, s15
	v_cvt_pk_fp8_f32 v14, v12, v13 op_sel:[0,0,1]
	s_sext_i32_i16 s14, s14
	v_mul_f32_e32 v6, 0x42800000, v30
	v_mul_f32_e32 v9, 0x42800000, v34
	v_cvt_pk_fp8_f32 v10, v6, v9 op_sel:[0,0,1]
	v_mul_f32_e32 v4, 0x42800000, v31
	v_mul_f32_e32 v5, 0x42800000, v35
	s_lshl_b32 s14, s14, 3
	v_cvt_pk_fp8_f32 v7, v4, v5 op_sel:[0,0,1]
	v_lshlrev_b32_e32 v1, 4, v1
	s_and_b32 s14, s14, 0xffffff80
	ds_write2_b32 v2, v101, v14 offset1:16
	ds_write2_b32 v2, v17, v8 offset0:36 offset1:52
	ds_write2_b32 v2, v18, v10 offset0:72 offset1:88
	ds_write2_b32 v2, v15, v7 offset0:108 offset1:124
	v_and_b32_e32 v2, 0x70, v1
	s_ashr_i32 s15, s14, 31
	v_mul_lo_u32 v1, v100, s91
	s_add_u32 s14, s16, s14
	v_add3_u32 v1, 0, v2, v1
	s_waitcnt lgkmcnt(0)
	s_barrier
	s_addc_u32 s15, s17, s15
	ds_read_b128 v[4:7], v1
	v_ashrrev_i32_e32 v101, 31, v100
	v_lshl_add_u64 v[8:9], s[14:15], 0, v[2:3]
	v_lshlrev_b64 v[10:11], 11, v[100:101]
	v_lshl_add_u64 v[12:13], v[8:9], 0, v[10:11]
	ds_read_b128 v[8:11], v1 offset:9216
	s_waitcnt lgkmcnt(1)
	global_store_dwordx4 v[12:13], v[4:7], off
	s_add_i32 s7, s7, 1
	s_addk_i32 s4, 0xc0
	v_add_co_u32_e32 v4, vcc, 0x20000, v12
	v_mov_b64_e32 v[16:17], v[68:69]
	s_nop 0
	v_addc_co_u32_e32 v5, vcc, 0, v13, vcc
	s_waitcnt lgkmcnt(0)
	global_store_dwordx4 v[4:5], v[8:11], off
	v_mov_b64_e32 v[12:13], v[80:81]
	v_mov_b64_e32 v[20:21], v[64:65]
	v_mov_b64_e32 v[24:25], v[60:61]
	v_mov_b64_e32 v[4:5], v[56:57]
	v_mov_b64_e32 v[8:9], v[52:53]
	v_mov_b64_e32 v[28:29], v[48:49]
	v_mov_b64_e32 v[32:33], v[44:45]
	s_cmp_lg_u32 s7, 15
	v_mov_b64_e32 v[14:15], v[82:83]
	v_mov_b64_e32 v[18:19], v[70:71]
	v_mov_b64_e32 v[22:23], v[66:67]
	v_mov_b64_e32 v[26:27], v[62:63]
	v_mov_b64_e32 v[6:7], v[58:59]
	v_mov_b64_e32 v[10:11], v[54:55]
	v_mov_b64_e32 v[30:31], v[50:51]
	v_mov_b64_e32 v[34:35], v[46:47]
	s_barrier
	s_cbranch_scc0 .LBB0_1174
; DEVI int opaque_tid() { int t = threadIdx.x; asm volatile("" : "+v"(t)); return t; }
; DEVI void cvt8_load(const Params& p, int L, int t, CvtIn& in) {
;     const int which = t / 4096, r = t % 4096, le = L * 16 + r / 256, kt = (r % 256) / 16, nt = r % 16;
;     const float* src = (which == 2 ? p.w_down : (which == 0 ? p.w_gate : p.w_up)) + (size_t)le * 2048 * 2048;
;     const int tid = opaque_tid(), nq = tid & 31, kq0 = tid >> 5;
; #pragma unroll
;     for (int it = 0; it < 2; ++it)
; #pragma unroll
;         for (int kk = 0; kk < 4; ++kk) in.v[it * 4 + kk] = __builtin_nontemporal_load((const f32x4*)(src + (size_t)(kt * 128 + (kq0 + it * 16) * 4 + kk) * 2048 + nt * 128 + nq * 4));
; }
; DEVI void cvt8_stream3(const Params& p, int L, int t0, int step, int count, char* smem) {
;     ...
; #pragma nounroll
;     for (int i = 0; i < count; ++i) { CvtIn c;
;         if (i + 2 < count) cvt8_load(p, L, t0 + (i + 2) * step, c);
;         cvt8_finish(p, L, t0 + i * step, a, smem);
;         a = b; b = c; }
.LBB0_1168:
	s_waitcnt vmcnt(0)
	v_mov_b64_e32 v[44:45], v[96:97]
	v_mov_b64_e32 v[48:49], v[92:93]
	v_mov_b64_e32 v[52:53], v[88:89]
	v_mov_b64_e32 v[56:57], v[84:85]
	v_mov_b64_e32 v[60:61], v[76:77]
	v_mov_b64_e32 v[64:65], v[72:73]
	v_mov_b64_e32 v[70:71], v[42:43]
	v_mov_b64_e32 v[82:83], v[38:39]
	v_mov_b64_e32 v[46:47], v[98:99]
	v_mov_b64_e32 v[50:51], v[94:95]
	v_mov_b64_e32 v[54:55], v[90:91]
	v_mov_b64_e32 v[58:59], v[86:87]
	v_mov_b64_e32 v[62:63], v[78:79]
	v_mov_b64_e32 v[66:67], v[74:75]
	v_mov_b64_e32 v[68:69], v[40:41]
	s_cmp_gt_u32 s7, 12
	v_mov_b64_e32 v[80:81], v[36:37]
	s_cbranch_scc1 .LBB0_1170
	s_add_i32 s16, s4, 0x180
	s_and_b32 s14, s16, 0xfffff000
	s_cmpk_lt_u32 s16, 0x1000
	s_cselect_b32 s15, s64, 0x80
	s_cmpk_lg_i32 s14, 0x2000
	s_cselect_b32 s14, s15, 0x88
	s_add_u32 s14, s0, s14
	s_addc_u32 s15, s1, 0
	s_ashr_i32 s17, s16, 31
	s_lshr_b32 s17, s17, 20
	s_add_i32 s17, s16, s17
	s_and_b32 s17, s17, 0xf000
	s_sub_i32 s16, s16, s17
	s_sext_i32_i16 s17, s16
	s_lshr_b32 s17, s17, 15
	s_bfe_u32 s18, s17, 0x4000c
	s_bfe_u32 s17, s17, 0x80008
	s_add_i32 s18, s16, s18
	s_add_i32 s17, s16, s17
	s_and_b32 s18, s18, 0xfff0
	s_sext_i32_i16 s19, s17
	s_and_b32 s17, s17, 0xff00
	s_sub_i32 s18, s16, s18
	s_sub_i32 s16, s16, s17
	s_sext_i32_i16 s17, s16
	s_bfe_u32 s17, s17, 0x4001b
	s_add_i32 s16, s16, s17
	s_load_dwordx2 s[14:15], s[14:15], 0x0
	s_sext_i32_i16 s23, s16
	s_ashr_i32 s16, s19, 8
	s_add_i32 s16, s5, s16
	s_ashr_i32 s17, s16, 31
	s_lshl_b64 s[16:17], s[16:17], 24
	s_waitcnt lgkmcnt(0)
	s_add_u32 s16, s14, s16
	v_mov_b32_e32 v1, v0
	s_addc_u32 s17, s15, s17
	s_lshl_b32 s14, s23, 3
	v_ashrrev_i32_e32 v2, 3, v1
	s_sext_i32_i16 s18, s18
	s_and_b32 s14, s14, 0xffffff80
	v_and_b32_e32 v2, -4, v2
	v_add_u32_e32 v72, s14, v2
	s_lshl_b32 s14, s18, 7
	s_ashr_i32 s15, s14, 31
	s_lshl_b64 s[14:15], s[14:15], 2
	s_add_u32 s14, s16, s14
	v_lshlrev_b32_e32 v1, 4, v1
	s_addc_u32 s15, s17, s15
	v_and_b32_e32 v2, 0x1f0, v1
	v_ashrrev_i32_e32 v73, 31, v72
	v_lshl_add_u64 v[74:75], s[14:15], 0, v[2:3]
	v_lshlrev_b64 v[36:37], 13, v[72:73]
	v_lshl_add_u64 v[92:93], v[74:75], 0, v[36:37]
	v_add_co_u32_e32 v84, vcc, s94, v92
	v_or_b32_e32 v36, 1, v72
	s_nop 0
	v_addc_co_u32_e32 v85, vcc, 0, v93, vcc
	v_add_co_u32_e32 v88, vcc, 0x82000, v92
	v_or_b32_e32 v76, 2, v72
	s_nop 0
	v_addc_co_u32_e32 v89, vcc, 0, v93, vcc
	v_or_b32_e32 v72, 3, v72
	v_add_co_u32_e32 v94, vcc, 0x84000, v92
	v_ashrrev_i32_e32 v37, 31, v36
	v_ashrrev_i32_e32 v77, 31, v76
	v_ashrrev_i32_e32 v73, 31, v72
	v_addc_co_u32_e32 v95, vcc, 0, v93, vcc
	v_lshlrev_b64 v[36:37], 13, v[36:37]
	v_lshlrev_b64 v[76:77], 13, v[76:77]
	v_lshlrev_b64 v[72:73], 13, v[72:73]
	v_add_co_u32_e32 v96, vcc, 0x86000, v92
	v_lshl_add_u64 v[40:41], v[74:75], 0, v[36:37]
	v_lshl_add_u64 v[76:77], v[74:75], 0, v[76:77]
	v_lshl_add_u64 v[78:79], v[74:75], 0, v[72:73]
	v_addc_co_u32_e32 v97, vcc, 0, v93, vcc
	global_load_dwordx4 v[36:39], v[92:93], off nt
	s_nop 0
	global_load_dwordx4 v[40:43], v[40:41], off nt
	s_nop 0
	global_load_dwordx4 v[72:75], v[76:77], off nt
	s_nop 0
	global_load_dwordx4 v[76:79], v[78:79], off nt
	s_nop 0
	global_load_dwordx4 v[84:87], v[84:85], off nt
	s_nop 0
	global_load_dwordx4 v[88:91], v[88:89], off nt
	s_nop 0
	global_load_dwordx4 v[92:95], v[94:95], off nt
	s_nop 0
	global_load_dwordx4 v[96:99], v[96:97], off nt
